# scan wave: fourth decay-weight load issued with the other weight loads, one counted wait fewer per pair-step
# speedup vs baseline: 1.0128x; 1.0128x over previous
; #define LAS __attribute__((address_space(3)))
; __device__ __forceinline__ void scan_head(const Params& p, LAS unsigned char* lds, int bh, const int wave) {
;     ...
;         if (wave < 4) {
;             __builtin_amdgcn_s_setprio(3);
;             const int bp = chunk & 1, vb = chunk % 3;
;             const LAS unsigned char* awp = lds + L_AW + bp * 8192 + sel * 128 + rg * 16;
;             const LAS unsigned char* wwp = lds + L_W + bp * 8192 + rg * 16;
;             const LAS unsigned char* abp = lds + L_BK + bp * 16384 + rg * 256 + ri * 4;
;             const LAS unsigned char* vp = lds + L_V + vb * 8192 + (16 * wave + ri) * 4;
;             const LAS unsigned char* csp = lds + L_CS + bp * 256;
;             LAS unsigned char* yp = (rg == 0) ? (lds + L_Y + bp * 8192 + (16 * wave + ri) * 4) : ((rg == 2) ? (lds + L_Y + bp * 8192 + 256 + (16 * wave + ri) * 4) : (lds + L_DUMMY + tid * 4));
;             const int y_st = (rg & 1) ? 0 : 512;
;     ...
;             bf16x8 Pa0, Pa1, Qa0, Qa1; f32x4 Pw0, Pw1, Pw2, Pw3, Qw0, Qw1, Qw2, Qw3, Pcs, Qcs; float Pb0, Pb1, Pb2, Pb3, Pvt, Pvu, Qb0, Qb1, Qb2, Qb3, Qvt, Qvu;
;             SCAN_LD(P, 0);
; #pragma unroll 1
;             for (int pi = 0; pi < 16; pi += 2) {
;                 SCAN_LD(Q, pi + 1);
;                 SCAN_STEP(P, pi);
;                 if (pi + 2 < 16) SCAN_LD(P, pi + 2);
;                 SCAN_STEP(Q, pi + 1);
.LBB0_806:
	s_and_b64 vcc, exec, s[14:15]
	s_cbranch_vccz .LBB0_789
	s_setprio 3
	s_and_b32 s2, s51, 1
	s_lshl_b32 s15, s2, 13
	s_mul_i32 s14, s51, 0xab
	s_lshl_b32 s52, s2, 14
	s_bfe_u32 s14, s14, 0x70009
	s_lshl_b32 s44, s2, 8
	s_mul_i32 s14, s14, 3
	s_waitcnt vmcnt(0)
	s_sub_i32 s14, s51, s14
	s_and_b32 s14, s14, 0xff
	s_lshl_b32 s14, s14, 13
	s_add_i32 s44, s44, 0x20300
	v_add_u32_e32 v98, s15, v176
	v_add_u32_e32 v99, s15, v175
	v_add_u32_e32 v0, s52, v178
	v_add_u32_e32 v1, s14, v179
	v_add_u32_e32 v0, 0x8000, v0
	v_add_u32_e32 v4, 0x100, v1
	v_mov_b32_e32 v2, s44
	v_cndmask_b32_e64 v4, v4, v1, s[8:9]
	v_cndmask_b32_e64 v4, v4, v1, s[12:13]
	v_cndmask_b32_e64 v1, v4, v1, s[10:11]
	v_add_u32_e32 v4, s15, v181
	v_add_u32_e32 v6, 0xd00, v180
	v_add_u32_e32 v5, 0x100, v4
	v_cndmask_b32_e64 v5, v6, v5, s[10:11]
	v_cndmask_b32_e64 v3, v5, v4, s[8:9]
	ds_read_b128 v[68:71], v98 offset:0
	ds_read_b128 v[72:75], v98 offset:64
	ds_read_b128 v[76:79], v99 offset:16384
	ds_read_b128 v[80:83], v99 offset:16448
	ds_read_b128 v[84:87], v99 offset:16512
	ds_read_b128 v[88:91], v99 offset:16576
	ds_read2_b32 v[92:93], v0 offset1:16
	ds_read2_b32 v[94:95], v0 offset0:32 offset1:48
	ds_read_b32 v96, v1 offset:0
	ds_read_b128 v[100:103], v2 offset:0
	v_cvt_pk_bf16_f32 v8, v64, v65
	v_cvt_pk_bf16_f32 v9, v66, v67
	v_cvt_pk_bf16_f32 v10, v60, v61
	v_cvt_pk_bf16_f32 v11, v62, v63
	v_cvt_pk_bf16_f32 v12, v52, v53
	v_cvt_pk_bf16_f32 v13, v54, v55
	s_waitcnt lgkmcnt(4)
	v_mfma_f32_16x16x32_bf16 v[140:143], v[68:71], v[8:11], 0
	v_cvt_pk_bf16_f32 v14, v56, v57
	v_cvt_pk_bf16_f32 v15, v58, v59
	v_pk_mul_f32 v[64:65], v[64:65], v[76:77]
	v_pk_mul_f32 v[66:67], v[66:67], v[78:79]
	v_mfma_f32_16x16x32_bf16 v[140:143], v[72:75], v[12:15], v[140:143]
	v_pk_mul_f32 v[60:61], v[60:61], v[80:81]
	v_pk_mul_f32 v[62:63], v[62:63], v[82:83]
	v_pk_mul_f32 v[52:53], v[52:53], v[84:85]
	v_pk_mul_f32 v[54:55], v[54:55], v[86:87]
	v_pk_mul_f32 v[56:57], v[56:57], v[88:89]
	v_pk_mul_f32 v[58:59], v[58:59], v[90:91]
	ds_read_b128 v[104:107], v98 offset:512
	ds_read_b128 v[108:111], v98 offset:576
	ds_read_b128 v[112:115], v99 offset:16640
	ds_read_b128 v[116:119], v99 offset:16704
	ds_read_b128 v[120:123], v99 offset:16768
	ds_read_b128 v[128:131], v99 offset:16832
	s_waitcnt lgkmcnt(6)
	v_fma_f32 v144, v100, v140, v142
	v_fmac_f32_e32 v144, v101, v96
	v_cndmask_b32_e64 v145, v96, v144, s[10:11]
	v_cndmask_b32_e64 v145, v145, v140, s[8:9]
	v_fma_f32 v50, v102, v140, v143
	v_fmac_f32_e32 v50, v103, v96
	v_mfma_f32_16x16x4_f32 v[64:67], v92, v145, v[64:67]
	v_mfma_f32_16x16x4_f32 v[60:63], v93, v145, v[60:63]
	v_mfma_f32_16x16x4_f32 v[52:55], v94, v145, v[52:55]
	v_mfma_f32_16x16x4_f32 v[56:59], v95, v145, v[56:59]
	v_cndmask_b32_e64 v50, v50, v141, s[8:9]
	ds_write_b32 v3, v50 offset:0
	v_add_u32_e32 v0, 0x400, v0
	ds_read2_b32 v[132:133], v0 offset1:16
	ds_read2_b32 v[134:135], v0 offset0:32 offset1:48
	ds_read_b32 v97, v1 offset:512
	ds_read_b128 v[136:139], v2 offset:16
	v_cvt_pk_bf16_f32 v8, v64, v65
	v_cvt_pk_bf16_f32 v9, v66, v67
	v_cvt_pk_bf16_f32 v10, v60, v61
	v_cvt_pk_bf16_f32 v11, v62, v63
	v_cvt_pk_bf16_f32 v12, v52, v53
	v_cvt_pk_bf16_f32 v13, v54, v55
	s_waitcnt lgkmcnt(4)
	v_mfma_f32_16x16x32_bf16 v[140:143], v[104:107], v[8:11], 0
	v_cvt_pk_bf16_f32 v14, v56, v57
	v_cvt_pk_bf16_f32 v15, v58, v59
	v_pk_mul_f32 v[64:65], v[64:65], v[112:113]
	v_pk_mul_f32 v[66:67], v[66:67], v[114:115]
	v_mfma_f32_16x16x32_bf16 v[140:143], v[108:111], v[12:15], v[140:143]
	v_pk_mul_f32 v[60:61], v[60:61], v[116:117]
	v_pk_mul_f32 v[62:63], v[62:63], v[118:119]
	v_pk_mul_f32 v[52:53], v[52:53], v[120:121]
	v_pk_mul_f32 v[54:55], v[54:55], v[122:123]
	v_pk_mul_f32 v[56:57], v[56:57], v[128:129]
	v_pk_mul_f32 v[58:59], v[58:59], v[130:131]
	ds_read_b128 v[68:71], v98 offset:1024
	ds_read_b128 v[72:75], v98 offset:1088
	ds_read_b128 v[76:79], v99 offset:16896
	ds_read_b128 v[80:83], v99 offset:16960
	ds_read_b128 v[84:87], v99 offset:17024
	ds_read_b128 v[88:91], v99 offset:17088
	s_waitcnt lgkmcnt(6)
	v_fma_f32 v144, v136, v140, v142
	v_fmac_f32_e32 v144, v137, v97
	v_cndmask_b32_e64 v145, v97, v144, s[10:11]
	v_cndmask_b32_e64 v145, v145, v140, s[8:9]
	v_fma_f32 v50, v138, v140, v143
	v_fmac_f32_e32 v50, v139, v97
	v_mfma_f32_16x16x4_f32 v[64:67], v132, v145, v[64:67]
	v_mfma_f32_16x16x4_f32 v[60:63], v133, v145, v[60:63]
	v_mfma_f32_16x16x4_f32 v[52:55], v134, v145, v[52:55]
	v_mfma_f32_16x16x4_f32 v[56:59], v135, v145, v[56:59]
	v_cndmask_b32_e64 v50, v50, v141, s[8:9]
	ds_write_b32 v3, v50 offset:512
	v_add_u32_e32 v0, 0x400, v0
	ds_read2_b32 v[92:93], v0 offset1:16
	ds_read2_b32 v[94:95], v0 offset0:32 offset1:48
	ds_read_b32 v96, v1 offset:1024
	ds_read_b128 v[100:103], v2 offset:32
	v_cvt_pk_bf16_f32 v8, v64, v65
	v_cvt_pk_bf16_f32 v9, v66, v67
	v_cvt_pk_bf16_f32 v10, v60, v61
	v_cvt_pk_bf16_f32 v11, v62, v63
	v_cvt_pk_bf16_f32 v12, v52, v53
	v_cvt_pk_bf16_f32 v13, v54, v55
	s_waitcnt lgkmcnt(4)
	v_mfma_f32_16x16x32_bf16 v[140:143], v[68:71], v[8:11], 0
	v_cvt_pk_bf16_f32 v14, v56, v57
	v_cvt_pk_bf16_f32 v15, v58, v59
	v_pk_mul_f32 v[64:65], v[64:65], v[76:77]
	v_pk_mul_f32 v[66:67], v[66:67], v[78:79]
	v_mfma_f32_16x16x32_bf16 v[140:143], v[72:75], v[12:15], v[140:143]
	v_pk_mul_f32 v[60:61], v[60:61], v[80:81]
	v_pk_mul_f32 v[62:63], v[62:63], v[82:83]
	v_pk_mul_f32 v[52:53], v[52:53], v[84:85]
	v_pk_mul_f32 v[54:55], v[54:55], v[86:87]
	v_pk_mul_f32 v[56:57], v[56:57], v[88:89]
	v_pk_mul_f32 v[58:59], v[58:59], v[90:91]
	ds_read_b128 v[104:107], v98 offset:1536
	ds_read_b128 v[108:111], v98 offset:1600
	ds_read_b128 v[112:115], v99 offset:17152
	ds_read_b128 v[116:119], v99 offset:17216
	ds_read_b128 v[120:123], v99 offset:17280
	ds_read_b128 v[128:131], v99 offset:17344
	s_waitcnt lgkmcnt(6)
; __device__ __forceinline__ void scan_head(const Params& p, LAS unsigned char* lds, int bh, const int wave) {
;     ...
;             bf16x8 Pa0, Pa1, Qa0, Qa1; f32x4 Pw0, Pw1, Pw2, Pw3, Qw0, Qw1, Qw2, Qw3, Pcs, Qcs; float Pb0, Pb1, Pb2, Pb3, Pvt, Pvu, Qb0, Qb1, Qb2, Qb3, Qvt, Qvu;
;             SCAN_LD(P, 0);
; #pragma unroll 1
;             for (int pi = 0; pi < 16; pi += 2) {
;                 SCAN_LD(Q, pi + 1);
;                 SCAN_STEP(P, pi);
;                 if (pi + 2 < 16) SCAN_LD(P, pi + 2);
;                 SCAN_STEP(Q, pi + 1);
	v_fma_f32 v144, v100, v140, v142
	v_fmac_f32_e32 v144, v101, v96
	v_cndmask_b32_e64 v145, v96, v144, s[10:11]
	v_cndmask_b32_e64 v145, v145, v140, s[8:9]
	v_fma_f32 v50, v102, v140, v143
	v_fmac_f32_e32 v50, v103, v96
	v_mfma_f32_16x16x4_f32 v[64:67], v92, v145, v[64:67]
	v_mfma_f32_16x16x4_f32 v[60:63], v93, v145, v[60:63]
	v_mfma_f32_16x16x4_f32 v[52:55], v94, v145, v[52:55]
	v_mfma_f32_16x16x4_f32 v[56:59], v95, v145, v[56:59]
	v_cndmask_b32_e64 v50, v50, v141, s[8:9]
	ds_write_b32 v3, v50 offset:1024
	v_add_u32_e32 v0, 0x400, v0
	ds_read2_b32 v[132:133], v0 offset1:16
	ds_read2_b32 v[134:135], v0 offset0:32 offset1:48
	ds_read_b32 v97, v1 offset:1536
	ds_read_b128 v[136:139], v2 offset:48
	v_cvt_pk_bf16_f32 v8, v64, v65
	v_cvt_pk_bf16_f32 v9, v66, v67
	v_cvt_pk_bf16_f32 v10, v60, v61
	v_cvt_pk_bf16_f32 v11, v62, v63
	v_cvt_pk_bf16_f32 v12, v52, v53
	v_cvt_pk_bf16_f32 v13, v54, v55
	s_waitcnt lgkmcnt(4)
	v_mfma_f32_16x16x32_bf16 v[140:143], v[104:107], v[8:11], 0
	v_cvt_pk_bf16_f32 v14, v56, v57
	v_cvt_pk_bf16_f32 v15, v58, v59
	v_pk_mul_f32 v[64:65], v[64:65], v[112:113]
	v_pk_mul_f32 v[66:67], v[66:67], v[114:115]
	v_mfma_f32_16x16x32_bf16 v[140:143], v[108:111], v[12:15], v[140:143]
	v_pk_mul_f32 v[60:61], v[60:61], v[116:117]
	v_pk_mul_f32 v[62:63], v[62:63], v[118:119]
	v_pk_mul_f32 v[52:53], v[52:53], v[120:121]
	v_pk_mul_f32 v[54:55], v[54:55], v[122:123]
	v_pk_mul_f32 v[56:57], v[56:57], v[128:129]
	v_pk_mul_f32 v[58:59], v[58:59], v[130:131]
	ds_read_b128 v[68:71], v98 offset:2048
	ds_read_b128 v[72:75], v98 offset:2112
	ds_read_b128 v[76:79], v99 offset:17408
	ds_read_b128 v[80:83], v99 offset:17472
	ds_read_b128 v[84:87], v99 offset:17536
	ds_read_b128 v[88:91], v99 offset:17600
	s_waitcnt lgkmcnt(6)
	v_fma_f32 v144, v136, v140, v142
	v_fmac_f32_e32 v144, v137, v97
	v_cndmask_b32_e64 v145, v97, v144, s[10:11]
	v_cndmask_b32_e64 v145, v145, v140, s[8:9]
	v_fma_f32 v50, v138, v140, v143
	v_fmac_f32_e32 v50, v139, v97
	v_mfma_f32_16x16x4_f32 v[64:67], v132, v145, v[64:67]
	v_mfma_f32_16x16x4_f32 v[60:63], v133, v145, v[60:63]
	v_mfma_f32_16x16x4_f32 v[52:55], v134, v145, v[52:55]
	v_mfma_f32_16x16x4_f32 v[56:59], v135, v145, v[56:59]
	v_cndmask_b32_e64 v50, v50, v141, s[8:9]
	ds_write_b32 v3, v50 offset:1536
	v_add_u32_e32 v0, 0x400, v0
	ds_read2_b32 v[92:93], v0 offset1:16
	ds_read2_b32 v[94:95], v0 offset0:32 offset1:48
	ds_read_b32 v96, v1 offset:2048
	ds_read_b128 v[100:103], v2 offset:64
	v_cvt_pk_bf16_f32 v8, v64, v65
	v_cvt_pk_bf16_f32 v9, v66, v67
	v_cvt_pk_bf16_f32 v10, v60, v61
	v_cvt_pk_bf16_f32 v11, v62, v63
	v_cvt_pk_bf16_f32 v12, v52, v53
	v_cvt_pk_bf16_f32 v13, v54, v55
	s_waitcnt lgkmcnt(4)
	v_mfma_f32_16x16x32_bf16 v[140:143], v[68:71], v[8:11], 0
	v_cvt_pk_bf16_f32 v14, v56, v57
	v_cvt_pk_bf16_f32 v15, v58, v59
	v_pk_mul_f32 v[64:65], v[64:65], v[76:77]
	v_pk_mul_f32 v[66:67], v[66:67], v[78:79]
	v_mfma_f32_16x16x32_bf16 v[140:143], v[72:75], v[12:15], v[140:143]
	v_pk_mul_f32 v[60:61], v[60:61], v[80:81]
	v_pk_mul_f32 v[62:63], v[62:63], v[82:83]
	v_pk_mul_f32 v[52:53], v[52:53], v[84:85]
	v_pk_mul_f32 v[54:55], v[54:55], v[86:87]
	v_pk_mul_f32 v[56:57], v[56:57], v[88:89]
	v_pk_mul_f32 v[58:59], v[58:59], v[90:91]
	ds_read_b128 v[104:107], v98 offset:2560
	ds_read_b128 v[108:111], v98 offset:2624
	ds_read_b128 v[112:115], v99 offset:17664
	ds_read_b128 v[116:119], v99 offset:17728
	ds_read_b128 v[120:123], v99 offset:17792
	ds_read_b128 v[128:131], v99 offset:17856
	s_waitcnt lgkmcnt(6)
	v_fma_f32 v144, v100, v140, v142
	v_fmac_f32_e32 v144, v101, v96
	v_cndmask_b32_e64 v145, v96, v144, s[10:11]
	v_cndmask_b32_e64 v145, v145, v140, s[8:9]
	v_fma_f32 v50, v102, v140, v143
	v_fmac_f32_e32 v50, v103, v96
	v_mfma_f32_16x16x4_f32 v[64:67], v92, v145, v[64:67]
	v_mfma_f32_16x16x4_f32 v[60:63], v93, v145, v[60:63]
	v_mfma_f32_16x16x4_f32 v[52:55], v94, v145, v[52:55]
	v_mfma_f32_16x16x4_f32 v[56:59], v95, v145, v[56:59]
	v_cndmask_b32_e64 v50, v50, v141, s[8:9]
	ds_write_b32 v3, v50 offset:2048
	v_add_u32_e32 v0, 0x400, v0
	ds_read2_b32 v[132:133], v0 offset1:16
	ds_read2_b32 v[134:135], v0 offset0:32 offset1:48
	ds_read_b32 v97, v1 offset:2560
	ds_read_b128 v[136:139], v2 offset:80
	v_cvt_pk_bf16_f32 v8, v64, v65
	v_cvt_pk_bf16_f32 v9, v66, v67
	v_cvt_pk_bf16_f32 v10, v60, v61
	v_cvt_pk_bf16_f32 v11, v62, v63
	v_cvt_pk_bf16_f32 v12, v52, v53
	v_cvt_pk_bf16_f32 v13, v54, v55
	s_waitcnt lgkmcnt(4)
	v_mfma_f32_16x16x32_bf16 v[140:143], v[104:107], v[8:11], 0
	v_cvt_pk_bf16_f32 v14, v56, v57
	v_cvt_pk_bf16_f32 v15, v58, v59
	v_pk_mul_f32 v[64:65], v[64:65], v[112:113]
	v_pk_mul_f32 v[66:67], v[66:67], v[114:115]
	v_mfma_f32_16x16x32_bf16 v[140:143], v[108:111], v[12:15], v[140:143]
	v_pk_mul_f32 v[60:61], v[60:61], v[116:117]
	v_pk_mul_f32 v[62:63], v[62:63], v[118:119]
	v_pk_mul_f32 v[52:53], v[52:53], v[120:121]
	v_pk_mul_f32 v[54:55], v[54:55], v[122:123]
	v_pk_mul_f32 v[56:57], v[56:57], v[128:129]
	v_pk_mul_f32 v[58:59], v[58:59], v[130:131]
	ds_read_b128 v[68:71], v98 offset:3072
	ds_read_b128 v[72:75], v98 offset:3136
	ds_read_b128 v[76:79], v99 offset:17920
	ds_read_b128 v[80:83], v99 offset:17984
	ds_read_b128 v[84:87], v99 offset:18048
	ds_read_b128 v[88:91], v99 offset:18112
	s_waitcnt lgkmcnt(6)
; __device__ __forceinline__ void scan_head(const Params& p, LAS unsigned char* lds, int bh, const int wave) {
;     ...
;             bf16x8 Pa0, Pa1, Qa0, Qa1; f32x4 Pw0, Pw1, Pw2, Pw3, Qw0, Qw1, Qw2, Qw3, Pcs, Qcs; float Pb0, Pb1, Pb2, Pb3, Pvt, Pvu, Qb0, Qb1, Qb2, Qb3, Qvt, Qvu;
;             SCAN_LD(P, 0);
; #pragma unroll 1
;             for (int pi = 0; pi < 16; pi += 2) {
;                 SCAN_LD(Q, pi + 1);
;                 SCAN_STEP(P, pi);
;                 if (pi + 2 < 16) SCAN_LD(P, pi + 2);
;                 SCAN_STEP(Q, pi + 1);
	v_fma_f32 v144, v136, v140, v142
	v_fmac_f32_e32 v144, v137, v97
	v_cndmask_b32_e64 v145, v97, v144, s[10:11]
	v_cndmask_b32_e64 v145, v145, v140, s[8:9]
	v_fma_f32 v50, v138, v140, v143
	v_fmac_f32_e32 v50, v139, v97
	v_mfma_f32_16x16x4_f32 v[64:67], v132, v145, v[64:67]
	v_mfma_f32_16x16x4_f32 v[60:63], v133, v145, v[60:63]
	v_mfma_f32_16x16x4_f32 v[52:55], v134, v145, v[52:55]
	v_mfma_f32_16x16x4_f32 v[56:59], v135, v145, v[56:59]
	v_cndmask_b32_e64 v50, v50, v141, s[8:9]
	ds_write_b32 v3, v50 offset:2560
	v_add_u32_e32 v0, 0x400, v0
	ds_read2_b32 v[92:93], v0 offset1:16
	ds_read2_b32 v[94:95], v0 offset0:32 offset1:48
	ds_read_b32 v96, v1 offset:3072
	ds_read_b128 v[100:103], v2 offset:96
	v_cvt_pk_bf16_f32 v8, v64, v65
	v_cvt_pk_bf16_f32 v9, v66, v67
	v_cvt_pk_bf16_f32 v10, v60, v61
	v_cvt_pk_bf16_f32 v11, v62, v63
	v_cvt_pk_bf16_f32 v12, v52, v53
	v_cvt_pk_bf16_f32 v13, v54, v55
	s_waitcnt lgkmcnt(4)
	v_mfma_f32_16x16x32_bf16 v[140:143], v[68:71], v[8:11], 0
	v_cvt_pk_bf16_f32 v14, v56, v57
	v_cvt_pk_bf16_f32 v15, v58, v59
	v_pk_mul_f32 v[64:65], v[64:65], v[76:77]
	v_pk_mul_f32 v[66:67], v[66:67], v[78:79]
	v_mfma_f32_16x16x32_bf16 v[140:143], v[72:75], v[12:15], v[140:143]
	v_pk_mul_f32 v[60:61], v[60:61], v[80:81]
	v_pk_mul_f32 v[62:63], v[62:63], v[82:83]
	v_pk_mul_f32 v[52:53], v[52:53], v[84:85]
	v_pk_mul_f32 v[54:55], v[54:55], v[86:87]
	v_pk_mul_f32 v[56:57], v[56:57], v[88:89]
	v_pk_mul_f32 v[58:59], v[58:59], v[90:91]
	ds_read_b128 v[104:107], v98 offset:3584
	ds_read_b128 v[108:111], v98 offset:3648
	ds_read_b128 v[112:115], v99 offset:18176
	ds_read_b128 v[116:119], v99 offset:18240
	ds_read_b128 v[120:123], v99 offset:18304
	ds_read_b128 v[128:131], v99 offset:18368
	s_waitcnt lgkmcnt(6)
	v_fma_f32 v144, v100, v140, v142
	v_fmac_f32_e32 v144, v101, v96
	v_cndmask_b32_e64 v145, v96, v144, s[10:11]
	v_cndmask_b32_e64 v145, v145, v140, s[8:9]
	v_fma_f32 v50, v102, v140, v143
	v_fmac_f32_e32 v50, v103, v96
	v_mfma_f32_16x16x4_f32 v[64:67], v92, v145, v[64:67]
	v_mfma_f32_16x16x4_f32 v[60:63], v93, v145, v[60:63]
	v_mfma_f32_16x16x4_f32 v[52:55], v94, v145, v[52:55]
	v_mfma_f32_16x16x4_f32 v[56:59], v95, v145, v[56:59]
	v_cndmask_b32_e64 v50, v50, v141, s[8:9]
	ds_write_b32 v3, v50 offset:3072
	v_add_u32_e32 v0, 0x400, v0
	ds_read2_b32 v[132:133], v0 offset1:16
	ds_read2_b32 v[134:135], v0 offset0:32 offset1:48
	ds_read_b32 v97, v1 offset:3584
	ds_read_b128 v[136:139], v2 offset:112
	v_cvt_pk_bf16_f32 v8, v64, v65
	v_cvt_pk_bf16_f32 v9, v66, v67
	v_cvt_pk_bf16_f32 v10, v60, v61
	v_cvt_pk_bf16_f32 v11, v62, v63
	v_cvt_pk_bf16_f32 v12, v52, v53
	v_cvt_pk_bf16_f32 v13, v54, v55
	s_waitcnt lgkmcnt(4)
	v_mfma_f32_16x16x32_bf16 v[140:143], v[104:107], v[8:11], 0
	v_cvt_pk_bf16_f32 v14, v56, v57
	v_cvt_pk_bf16_f32 v15, v58, v59
	v_pk_mul_f32 v[64:65], v[64:65], v[112:113]
	v_pk_mul_f32 v[66:67], v[66:67], v[114:115]
	v_mfma_f32_16x16x32_bf16 v[140:143], v[108:111], v[12:15], v[140:143]
	v_pk_mul_f32 v[60:61], v[60:61], v[116:117]
	v_pk_mul_f32 v[62:63], v[62:63], v[118:119]
	v_pk_mul_f32 v[52:53], v[52:53], v[120:121]
	v_pk_mul_f32 v[54:55], v[54:55], v[122:123]
	v_pk_mul_f32 v[56:57], v[56:57], v[128:129]
	v_pk_mul_f32 v[58:59], v[58:59], v[130:131]
	ds_read_b128 v[68:71], v98 offset:4096
	ds_read_b128 v[72:75], v98 offset:4160
	ds_read_b128 v[76:79], v99 offset:18432
	ds_read_b128 v[80:83], v99 offset:18496
	ds_read_b128 v[84:87], v99 offset:18560
	ds_read_b128 v[88:91], v99 offset:18624
	s_waitcnt lgkmcnt(6)
	v_fma_f32 v144, v136, v140, v142
	v_fmac_f32_e32 v144, v137, v97
	v_cndmask_b32_e64 v145, v97, v144, s[10:11]
	v_cndmask_b32_e64 v145, v145, v140, s[8:9]
	v_fma_f32 v50, v138, v140, v143
	v_fmac_f32_e32 v50, v139, v97
	v_mfma_f32_16x16x4_f32 v[64:67], v132, v145, v[64:67]
	v_mfma_f32_16x16x4_f32 v[60:63], v133, v145, v[60:63]
	v_mfma_f32_16x16x4_f32 v[52:55], v134, v145, v[52:55]
	v_mfma_f32_16x16x4_f32 v[56:59], v135, v145, v[56:59]
	v_cndmask_b32_e64 v50, v50, v141, s[8:9]
	ds_write_b32 v3, v50 offset:3584
	v_add_u32_e32 v0, 0x400, v0
	ds_read2_b32 v[92:93], v0 offset1:16
	ds_read2_b32 v[94:95], v0 offset0:32 offset1:48
	ds_read_b32 v96, v1 offset:4096
	ds_read_b128 v[100:103], v2 offset:128
	v_cvt_pk_bf16_f32 v8, v64, v65
	v_cvt_pk_bf16_f32 v9, v66, v67
	v_cvt_pk_bf16_f32 v10, v60, v61
	v_cvt_pk_bf16_f32 v11, v62, v63
	v_cvt_pk_bf16_f32 v12, v52, v53
	v_cvt_pk_bf16_f32 v13, v54, v55
	s_waitcnt lgkmcnt(4)
	v_mfma_f32_16x16x32_bf16 v[140:143], v[68:71], v[8:11], 0
	v_cvt_pk_bf16_f32 v14, v56, v57
	v_cvt_pk_bf16_f32 v15, v58, v59
	v_pk_mul_f32 v[64:65], v[64:65], v[76:77]
	v_pk_mul_f32 v[66:67], v[66:67], v[78:79]
	v_mfma_f32_16x16x32_bf16 v[140:143], v[72:75], v[12:15], v[140:143]
	v_pk_mul_f32 v[60:61], v[60:61], v[80:81]
	v_pk_mul_f32 v[62:63], v[62:63], v[82:83]
	v_pk_mul_f32 v[52:53], v[52:53], v[84:85]
	v_pk_mul_f32 v[54:55], v[54:55], v[86:87]
	v_pk_mul_f32 v[56:57], v[56:57], v[88:89]
	v_pk_mul_f32 v[58:59], v[58:59], v[90:91]
	ds_read_b128 v[104:107], v98 offset:4608
	ds_read_b128 v[108:111], v98 offset:4672
	ds_read_b128 v[112:115], v99 offset:18688
	ds_read_b128 v[116:119], v99 offset:18752
	ds_read_b128 v[120:123], v99 offset:18816
	ds_read_b128 v[128:131], v99 offset:18880
	s_waitcnt lgkmcnt(6)
; __device__ __forceinline__ void scan_head(const Params& p, LAS unsigned char* lds, int bh, const int wave) {
;     ...
;             bf16x8 Pa0, Pa1, Qa0, Qa1; f32x4 Pw0, Pw1, Pw2, Pw3, Qw0, Qw1, Qw2, Qw3, Pcs, Qcs; float Pb0, Pb1, Pb2, Pb3, Pvt, Pvu, Qb0, Qb1, Qb2, Qb3, Qvt, Qvu;
;             SCAN_LD(P, 0);
; #pragma unroll 1
;             for (int pi = 0; pi < 16; pi += 2) {
;                 SCAN_LD(Q, pi + 1);
;                 SCAN_STEP(P, pi);
;                 if (pi + 2 < 16) SCAN_LD(P, pi + 2);
;                 SCAN_STEP(Q, pi + 1);
	v_fma_f32 v144, v100, v140, v142
	v_fmac_f32_e32 v144, v101, v96
	v_cndmask_b32_e64 v145, v96, v144, s[10:11]
	v_cndmask_b32_e64 v145, v145, v140, s[8:9]
	v_fma_f32 v50, v102, v140, v143
	v_fmac_f32_e32 v50, v103, v96
	v_mfma_f32_16x16x4_f32 v[64:67], v92, v145, v[64:67]
	v_mfma_f32_16x16x4_f32 v[60:63], v93, v145, v[60:63]
	v_mfma_f32_16x16x4_f32 v[52:55], v94, v145, v[52:55]
	v_mfma_f32_16x16x4_f32 v[56:59], v95, v145, v[56:59]
	v_cndmask_b32_e64 v50, v50, v141, s[8:9]
	ds_write_b32 v3, v50 offset:4096
	v_add_u32_e32 v0, 0x400, v0
	ds_read2_b32 v[132:133], v0 offset1:16
	ds_read2_b32 v[134:135], v0 offset0:32 offset1:48
	ds_read_b32 v97, v1 offset:4608
	ds_read_b128 v[136:139], v2 offset:144
	v_cvt_pk_bf16_f32 v8, v64, v65
	v_cvt_pk_bf16_f32 v9, v66, v67
	v_cvt_pk_bf16_f32 v10, v60, v61
	v_cvt_pk_bf16_f32 v11, v62, v63
	v_cvt_pk_bf16_f32 v12, v52, v53
	v_cvt_pk_bf16_f32 v13, v54, v55
	s_waitcnt lgkmcnt(4)
	v_mfma_f32_16x16x32_bf16 v[140:143], v[104:107], v[8:11], 0
	v_cvt_pk_bf16_f32 v14, v56, v57
	v_cvt_pk_bf16_f32 v15, v58, v59
	v_pk_mul_f32 v[64:65], v[64:65], v[112:113]
	v_pk_mul_f32 v[66:67], v[66:67], v[114:115]
	v_mfma_f32_16x16x32_bf16 v[140:143], v[108:111], v[12:15], v[140:143]
	v_pk_mul_f32 v[60:61], v[60:61], v[116:117]
	v_pk_mul_f32 v[62:63], v[62:63], v[118:119]
	v_pk_mul_f32 v[52:53], v[52:53], v[120:121]
	v_pk_mul_f32 v[54:55], v[54:55], v[122:123]
	v_pk_mul_f32 v[56:57], v[56:57], v[128:129]
	v_pk_mul_f32 v[58:59], v[58:59], v[130:131]
	ds_read_b128 v[68:71], v98 offset:5120
	ds_read_b128 v[72:75], v98 offset:5184
	ds_read_b128 v[76:79], v99 offset:18944
	ds_read_b128 v[80:83], v99 offset:19008
	ds_read_b128 v[84:87], v99 offset:19072
	ds_read_b128 v[88:91], v99 offset:19136
	s_waitcnt lgkmcnt(6)
	v_fma_f32 v144, v136, v140, v142
	v_fmac_f32_e32 v144, v137, v97
	v_cndmask_b32_e64 v145, v97, v144, s[10:11]
	v_cndmask_b32_e64 v145, v145, v140, s[8:9]
	v_fma_f32 v50, v138, v140, v143
	v_fmac_f32_e32 v50, v139, v97
	v_mfma_f32_16x16x4_f32 v[64:67], v132, v145, v[64:67]
	v_mfma_f32_16x16x4_f32 v[60:63], v133, v145, v[60:63]
	v_mfma_f32_16x16x4_f32 v[52:55], v134, v145, v[52:55]
	v_mfma_f32_16x16x4_f32 v[56:59], v135, v145, v[56:59]
	v_cndmask_b32_e64 v50, v50, v141, s[8:9]
	ds_write_b32 v3, v50 offset:4608
	v_add_u32_e32 v0, 0x400, v0
	ds_read2_b32 v[92:93], v0 offset1:16
	ds_read2_b32 v[94:95], v0 offset0:32 offset1:48
	ds_read_b32 v96, v1 offset:5120
	ds_read_b128 v[100:103], v2 offset:160
	v_cvt_pk_bf16_f32 v8, v64, v65
	v_cvt_pk_bf16_f32 v9, v66, v67
	v_cvt_pk_bf16_f32 v10, v60, v61
	v_cvt_pk_bf16_f32 v11, v62, v63
	v_cvt_pk_bf16_f32 v12, v52, v53
	v_cvt_pk_bf16_f32 v13, v54, v55
	s_waitcnt lgkmcnt(4)
	v_mfma_f32_16x16x32_bf16 v[140:143], v[68:71], v[8:11], 0
	v_cvt_pk_bf16_f32 v14, v56, v57
	v_cvt_pk_bf16_f32 v15, v58, v59
	v_pk_mul_f32 v[64:65], v[64:65], v[76:77]
	v_pk_mul_f32 v[66:67], v[66:67], v[78:79]
	v_mfma_f32_16x16x32_bf16 v[140:143], v[72:75], v[12:15], v[140:143]
	v_pk_mul_f32 v[60:61], v[60:61], v[80:81]
	v_pk_mul_f32 v[62:63], v[62:63], v[82:83]
	v_pk_mul_f32 v[52:53], v[52:53], v[84:85]
	v_pk_mul_f32 v[54:55], v[54:55], v[86:87]
	v_pk_mul_f32 v[56:57], v[56:57], v[88:89]
	v_pk_mul_f32 v[58:59], v[58:59], v[90:91]
	ds_read_b128 v[104:107], v98 offset:5632
	ds_read_b128 v[108:111], v98 offset:5696
	ds_read_b128 v[112:115], v99 offset:19200
	ds_read_b128 v[116:119], v99 offset:19264
	ds_read_b128 v[120:123], v99 offset:19328
	ds_read_b128 v[128:131], v99 offset:19392
	s_waitcnt lgkmcnt(6)
	v_fma_f32 v144, v100, v140, v142
	v_fmac_f32_e32 v144, v101, v96
	v_cndmask_b32_e64 v145, v96, v144, s[10:11]
	v_cndmask_b32_e64 v145, v145, v140, s[8:9]
	v_fma_f32 v50, v102, v140, v143
	v_fmac_f32_e32 v50, v103, v96
	v_mfma_f32_16x16x4_f32 v[64:67], v92, v145, v[64:67]
	v_mfma_f32_16x16x4_f32 v[60:63], v93, v145, v[60:63]
	v_mfma_f32_16x16x4_f32 v[52:55], v94, v145, v[52:55]
	v_mfma_f32_16x16x4_f32 v[56:59], v95, v145, v[56:59]
	v_cndmask_b32_e64 v50, v50, v141, s[8:9]
	ds_write_b32 v3, v50 offset:5120
	v_add_u32_e32 v0, 0x400, v0
	ds_read2_b32 v[132:133], v0 offset1:16
	ds_read2_b32 v[134:135], v0 offset0:32 offset1:48
	ds_read_b32 v97, v1 offset:5632
	ds_read_b128 v[136:139], v2 offset:176
	v_cvt_pk_bf16_f32 v8, v64, v65
	v_cvt_pk_bf16_f32 v9, v66, v67
	v_cvt_pk_bf16_f32 v10, v60, v61
	v_cvt_pk_bf16_f32 v11, v62, v63
	v_cvt_pk_bf16_f32 v12, v52, v53
	v_cvt_pk_bf16_f32 v13, v54, v55
	s_waitcnt lgkmcnt(4)
	v_mfma_f32_16x16x32_bf16 v[140:143], v[104:107], v[8:11], 0
	v_cvt_pk_bf16_f32 v14, v56, v57
	v_cvt_pk_bf16_f32 v15, v58, v59
	v_pk_mul_f32 v[64:65], v[64:65], v[112:113]
	v_pk_mul_f32 v[66:67], v[66:67], v[114:115]
	v_mfma_f32_16x16x32_bf16 v[140:143], v[108:111], v[12:15], v[140:143]
	v_pk_mul_f32 v[60:61], v[60:61], v[116:117]
	v_pk_mul_f32 v[62:63], v[62:63], v[118:119]
	v_pk_mul_f32 v[52:53], v[52:53], v[120:121]
	v_pk_mul_f32 v[54:55], v[54:55], v[122:123]
	v_pk_mul_f32 v[56:57], v[56:57], v[128:129]
	v_pk_mul_f32 v[58:59], v[58:59], v[130:131]
	ds_read_b128 v[68:71], v98 offset:6144
	ds_read_b128 v[72:75], v98 offset:6208
	ds_read_b128 v[76:79], v99 offset:19456
	ds_read_b128 v[80:83], v99 offset:19520
	ds_read_b128 v[84:87], v99 offset:19584
	ds_read_b128 v[88:91], v99 offset:19648
	s_waitcnt lgkmcnt(6)
; __device__ __forceinline__ void scan_head(const Params& p, LAS unsigned char* lds, int bh, const int wave) {
;     ...
;             bf16x8 Pa0, Pa1, Qa0, Qa1; f32x4 Pw0, Pw1, Pw2, Pw3, Qw0, Qw1, Qw2, Qw3, Pcs, Qcs; float Pb0, Pb1, Pb2, Pb3, Pvt, Pvu, Qb0, Qb1, Qb2, Qb3, Qvt, Qvu;
;             SCAN_LD(P, 0);
; #pragma unroll 1
;             for (int pi = 0; pi < 16; pi += 2) {
;                 SCAN_LD(Q, pi + 1);
;                 SCAN_STEP(P, pi);
;                 if (pi + 2 < 16) SCAN_LD(P, pi + 2);
;                 SCAN_STEP(Q, pi + 1);
	v_fma_f32 v144, v136, v140, v142
	v_fmac_f32_e32 v144, v137, v97
	v_cndmask_b32_e64 v145, v97, v144, s[10:11]
	v_cndmask_b32_e64 v145, v145, v140, s[8:9]
	v_fma_f32 v50, v138, v140, v143
	v_fmac_f32_e32 v50, v139, v97
	v_mfma_f32_16x16x4_f32 v[64:67], v132, v145, v[64:67]
	v_mfma_f32_16x16x4_f32 v[60:63], v133, v145, v[60:63]
	v_mfma_f32_16x16x4_f32 v[52:55], v134, v145, v[52:55]
	v_mfma_f32_16x16x4_f32 v[56:59], v135, v145, v[56:59]
	v_cndmask_b32_e64 v50, v50, v141, s[8:9]
	ds_write_b32 v3, v50 offset:5632
	v_add_u32_e32 v0, 0x400, v0
	ds_read2_b32 v[92:93], v0 offset1:16
	ds_read2_b32 v[94:95], v0 offset0:32 offset1:48
	ds_read_b32 v96, v1 offset:6144
	ds_read_b128 v[100:103], v2 offset:192
	v_cvt_pk_bf16_f32 v8, v64, v65
	v_cvt_pk_bf16_f32 v9, v66, v67
	v_cvt_pk_bf16_f32 v10, v60, v61
	v_cvt_pk_bf16_f32 v11, v62, v63
	v_cvt_pk_bf16_f32 v12, v52, v53
	v_cvt_pk_bf16_f32 v13, v54, v55
	s_waitcnt lgkmcnt(4)
	v_mfma_f32_16x16x32_bf16 v[140:143], v[68:71], v[8:11], 0
	v_cvt_pk_bf16_f32 v14, v56, v57
	v_cvt_pk_bf16_f32 v15, v58, v59
	v_pk_mul_f32 v[64:65], v[64:65], v[76:77]
	v_pk_mul_f32 v[66:67], v[66:67], v[78:79]
	v_mfma_f32_16x16x32_bf16 v[140:143], v[72:75], v[12:15], v[140:143]
	v_pk_mul_f32 v[60:61], v[60:61], v[80:81]
	v_pk_mul_f32 v[62:63], v[62:63], v[82:83]
	v_pk_mul_f32 v[52:53], v[52:53], v[84:85]
	v_pk_mul_f32 v[54:55], v[54:55], v[86:87]
	v_pk_mul_f32 v[56:57], v[56:57], v[88:89]
	v_pk_mul_f32 v[58:59], v[58:59], v[90:91]
	ds_read_b128 v[104:107], v98 offset:6656
	ds_read_b128 v[108:111], v98 offset:6720
	ds_read_b128 v[112:115], v99 offset:19712
	ds_read_b128 v[116:119], v99 offset:19776
	ds_read_b128 v[120:123], v99 offset:19840
	ds_read_b128 v[128:131], v99 offset:19904
	s_waitcnt lgkmcnt(6)
	v_fma_f32 v144, v100, v140, v142
	v_fmac_f32_e32 v144, v101, v96
	v_cndmask_b32_e64 v145, v96, v144, s[10:11]
	v_cndmask_b32_e64 v145, v145, v140, s[8:9]
	v_fma_f32 v50, v102, v140, v143
	v_fmac_f32_e32 v50, v103, v96
	v_mfma_f32_16x16x4_f32 v[64:67], v92, v145, v[64:67]
	v_mfma_f32_16x16x4_f32 v[60:63], v93, v145, v[60:63]
	v_mfma_f32_16x16x4_f32 v[52:55], v94, v145, v[52:55]
	v_mfma_f32_16x16x4_f32 v[56:59], v95, v145, v[56:59]
	v_cndmask_b32_e64 v50, v50, v141, s[8:9]
	ds_write_b32 v3, v50 offset:6144
	v_add_u32_e32 v0, 0x400, v0
	ds_read2_b32 v[132:133], v0 offset1:16
	ds_read2_b32 v[134:135], v0 offset0:32 offset1:48
	ds_read_b32 v97, v1 offset:6656
	ds_read_b128 v[136:139], v2 offset:208
	v_cvt_pk_bf16_f32 v8, v64, v65
	v_cvt_pk_bf16_f32 v9, v66, v67
	v_cvt_pk_bf16_f32 v10, v60, v61
	v_cvt_pk_bf16_f32 v11, v62, v63
	v_cvt_pk_bf16_f32 v12, v52, v53
	v_cvt_pk_bf16_f32 v13, v54, v55
	s_waitcnt lgkmcnt(4)
	v_mfma_f32_16x16x32_bf16 v[140:143], v[104:107], v[8:11], 0
	v_cvt_pk_bf16_f32 v14, v56, v57
	v_cvt_pk_bf16_f32 v15, v58, v59
	v_pk_mul_f32 v[64:65], v[64:65], v[112:113]
	v_pk_mul_f32 v[66:67], v[66:67], v[114:115]
	v_mfma_f32_16x16x32_bf16 v[140:143], v[108:111], v[12:15], v[140:143]
	v_pk_mul_f32 v[60:61], v[60:61], v[116:117]
	v_pk_mul_f32 v[62:63], v[62:63], v[118:119]
	v_pk_mul_f32 v[52:53], v[52:53], v[120:121]
	v_pk_mul_f32 v[54:55], v[54:55], v[122:123]
	v_pk_mul_f32 v[56:57], v[56:57], v[128:129]
	v_pk_mul_f32 v[58:59], v[58:59], v[130:131]
	ds_read_b128 v[68:71], v98 offset:7168
	ds_read_b128 v[72:75], v98 offset:7232
	ds_read_b128 v[76:79], v99 offset:19968
	ds_read_b128 v[80:83], v99 offset:20032
	ds_read_b128 v[84:87], v99 offset:20096
	ds_read_b128 v[88:91], v99 offset:20160
	s_waitcnt lgkmcnt(6)
; __device__ __forceinline__ void scan_head(const Params& p, LAS unsigned char* lds, int bh, const int wave) {
;     ...
;             bf16x8 Pa0, Pa1, Qa0, Qa1; f32x4 Pw0, Pw1, Pw2, Pw3, Qw0, Qw1, Qw2, Qw3, Pcs, Qcs; float Pb0, Pb1, Pb2, Pb3, Pvt, Pvu, Qb0, Qb1, Qb2, Qb3, Qvt, Qvu;
;             SCAN_LD(P, 0);
; #pragma unroll 1
;             for (int pi = 0; pi < 16; pi += 2) {
;                 SCAN_LD(Q, pi + 1);
;                 SCAN_STEP(P, pi);
;                 if (pi + 2 < 16) SCAN_LD(P, pi + 2);
;                 SCAN_STEP(Q, pi + 1);
;             }
	v_fma_f32 v144, v136, v140, v142
	v_fmac_f32_e32 v144, v137, v97
	v_cndmask_b32_e64 v145, v97, v144, s[10:11]
	v_cndmask_b32_e64 v145, v145, v140, s[8:9]
	v_fma_f32 v50, v138, v140, v143
	v_fmac_f32_e32 v50, v139, v97
	v_mfma_f32_16x16x4_f32 v[64:67], v132, v145, v[64:67]
	v_mfma_f32_16x16x4_f32 v[60:63], v133, v145, v[60:63]
	v_mfma_f32_16x16x4_f32 v[52:55], v134, v145, v[52:55]
	v_mfma_f32_16x16x4_f32 v[56:59], v135, v145, v[56:59]
	v_cndmask_b32_e64 v50, v50, v141, s[8:9]
	ds_write_b32 v3, v50 offset:6656
	v_add_u32_e32 v0, 0x400, v0
	ds_read2_b32 v[92:93], v0 offset1:16
	ds_read2_b32 v[94:95], v0 offset0:32 offset1:48
	ds_read_b32 v96, v1 offset:7168
	ds_read_b128 v[100:103], v2 offset:224
	v_cvt_pk_bf16_f32 v8, v64, v65
	v_cvt_pk_bf16_f32 v9, v66, v67
	v_cvt_pk_bf16_f32 v10, v60, v61
	v_cvt_pk_bf16_f32 v11, v62, v63
	v_cvt_pk_bf16_f32 v12, v52, v53
	v_cvt_pk_bf16_f32 v13, v54, v55
	s_waitcnt lgkmcnt(4)
	v_mfma_f32_16x16x32_bf16 v[140:143], v[68:71], v[8:11], 0
	v_cvt_pk_bf16_f32 v14, v56, v57
	v_cvt_pk_bf16_f32 v15, v58, v59
	v_pk_mul_f32 v[64:65], v[64:65], v[76:77]
	v_pk_mul_f32 v[66:67], v[66:67], v[78:79]
	v_mfma_f32_16x16x32_bf16 v[140:143], v[72:75], v[12:15], v[140:143]
	v_pk_mul_f32 v[60:61], v[60:61], v[80:81]
	v_pk_mul_f32 v[62:63], v[62:63], v[82:83]
	v_pk_mul_f32 v[52:53], v[52:53], v[84:85]
	v_pk_mul_f32 v[54:55], v[54:55], v[86:87]
	v_pk_mul_f32 v[56:57], v[56:57], v[88:89]
	v_pk_mul_f32 v[58:59], v[58:59], v[90:91]
	ds_read_b128 v[104:107], v98 offset:7680
	ds_read_b128 v[108:111], v98 offset:7744
	ds_read_b128 v[112:115], v99 offset:20224
	ds_read_b128 v[116:119], v99 offset:20288
	ds_read_b128 v[120:123], v99 offset:20352
	ds_read_b128 v[128:131], v99 offset:20416
	s_waitcnt lgkmcnt(6)
	v_fma_f32 v144, v100, v140, v142
	v_fmac_f32_e32 v144, v101, v96
	v_cndmask_b32_e64 v145, v96, v144, s[10:11]
	v_cndmask_b32_e64 v145, v145, v140, s[8:9]
	v_fma_f32 v50, v102, v140, v143
	v_fmac_f32_e32 v50, v103, v96
	v_mfma_f32_16x16x4_f32 v[64:67], v92, v145, v[64:67]
	v_mfma_f32_16x16x4_f32 v[60:63], v93, v145, v[60:63]
	v_mfma_f32_16x16x4_f32 v[52:55], v94, v145, v[52:55]
	v_mfma_f32_16x16x4_f32 v[56:59], v95, v145, v[56:59]
	v_cndmask_b32_e64 v50, v50, v141, s[8:9]
	ds_write_b32 v3, v50 offset:7168
	v_add_u32_e32 v0, 0x400, v0
	ds_read2_b32 v[132:133], v0 offset1:16
	ds_read2_b32 v[134:135], v0 offset0:32 offset1:48
	ds_read_b32 v97, v1 offset:7680
	ds_read_b128 v[136:139], v2 offset:240
	v_cvt_pk_bf16_f32 v8, v64, v65
	v_cvt_pk_bf16_f32 v9, v66, v67
	v_cvt_pk_bf16_f32 v10, v60, v61
	v_cvt_pk_bf16_f32 v11, v62, v63
	v_cvt_pk_bf16_f32 v12, v52, v53
	v_cvt_pk_bf16_f32 v13, v54, v55
	s_waitcnt lgkmcnt(4)
	v_mfma_f32_16x16x32_bf16 v[140:143], v[104:107], v[8:11], 0
	v_cvt_pk_bf16_f32 v14, v56, v57
	v_cvt_pk_bf16_f32 v15, v58, v59
	v_pk_mul_f32 v[64:65], v[64:65], v[112:113]
	v_pk_mul_f32 v[66:67], v[66:67], v[114:115]
	v_mfma_f32_16x16x32_bf16 v[140:143], v[108:111], v[12:15], v[140:143]
	v_pk_mul_f32 v[60:61], v[60:61], v[116:117]
	v_pk_mul_f32 v[62:63], v[62:63], v[118:119]
	v_pk_mul_f32 v[52:53], v[52:53], v[120:121]
	v_pk_mul_f32 v[54:55], v[54:55], v[122:123]
	v_pk_mul_f32 v[56:57], v[56:57], v[128:129]
	v_pk_mul_f32 v[58:59], v[58:59], v[130:131]
	s_waitcnt lgkmcnt(0)
	s_nop 1
	v_fma_f32 v144, v136, v140, v142
	v_fmac_f32_e32 v144, v137, v97
	v_cndmask_b32_e64 v145, v97, v144, s[10:11]
	v_cndmask_b32_e64 v145, v145, v140, s[8:9]
	v_fma_f32 v50, v138, v140, v143
	v_fmac_f32_e32 v50, v139, v97
	v_mfma_f32_16x16x4_f32 v[64:67], v132, v145, v[64:67]
	v_mfma_f32_16x16x4_f32 v[60:63], v133, v145, v[60:63]
	v_mfma_f32_16x16x4_f32 v[52:55], v134, v145, v[52:55]
	v_mfma_f32_16x16x4_f32 v[56:59], v135, v145, v[56:59]
	v_cndmask_b32_e64 v50, v50, v141, s[8:9]
	ds_write_b32 v3, v50 offset:7680
	s_nop 7
